# baseline (speedup 1.0000x reference)
.LBB9_34:
	v_and_b32_e32 v197, 15, v0
	v_bfe_u32 v198, v0, 4, 2
	s_bfe_u32 s62, s54, 0x20006
	s_lshr_b32 s63, s54, 8
	s_lshl_b32 s64, s63, 8
	s_add_u32 s64, s64, s53
	v_lshl_add_u32 v201, v198, 4, s64
	ds_read_b128 v[74:77], v201 offset:8192
	ds_read_b128 v[78:81], v201 offset:8256
	ds_read_b128 v[82:85], v201 offset:8320
	ds_read_b128 v[86:89], v201 offset:8384
	ds_read_b128 v[90:93], v201 offset:8704
	ds_read_b128 v[94:97], v201 offset:8768
	ds_read_b128 v[34:37], v201 offset:8832
	ds_read_b128 v[38:41], v201 offset:8896
	ds_read_b128 v[42:45], v201 offset:9216
	ds_read_b128 v[50:53], v201 offset:9280
	ds_read_b128 v[54:57], v201 offset:9344
	ds_read_b128 v[62:65], v201 offset:9408
	ds_read_b128 v[66:69], v201 offset:9728
	ds_read_b128 v[18:21], v201 offset:9792
	ds_read_b128 v[22:25], v201 offset:9856
	ds_read_b128 v[10:13], v201 offset:9920
	s_lshl_b32 s64, s62, 10
	s_add_u32 s64, s64, s53
	v_lshl_add_u32 v212, v197, 5, s64
	s_lshl_b32 s64, s62, 5
	s_add_u32 s64, s64, s52
	v_add_u32_e32 v194, s64, v197
	v_lshlrev_b32_e32 v194, 12, v194
	v_and_b32_e32 v199, 1, v198
	v_lshrrev_b32_e32 v209, 1, v198
	v_lshlrev_b32_e32 v199, 4, v199
	v_lshl_add_u32 v199, v209, 3, v199
	s_lshl_b32 s64, s63, 6
	s_add_u32 s64, s64, s38
	v_add_u32_e32 v199, s64, v199
	v_lshl_add_u32 v194, v199, 1, v194
	ds_read_b128 v[204:207], v212
	ds_read_b128 v[196:199], v212 offset:16
	v_mov_b32_e32 v210, v194
	s_waitcnt lgkmcnt(0)
	v_add_f32_e32 v204, v204, v206
	v_add_f32_e32 v196, v196, v198
	v_add_f32_e32 v204, v204, v196
	v_add_f32_e32 v205, v205, v207
	v_add_f32_e32 v197, v197, v199
	v_add_f32_e32 v205, v205, v197
	v_mul_f32_e32 v204, s36, v204
	v_mul_f32_e32 v205, s36, v205
	v_fma_f32 v205, -v204, v204, v205
	v_max_f32_e32 v205, 0, v205
	v_add_f32_e32 v205, 0x3727c5ac, v205
	v_rsq_f32_e32 v206, v205
	s_nop 0
	v_mul_f32_e64 v208, v206, -v204
	v_pk_fma_f32 v[196:197], v[208:209], v[74:75], v[42:43] op_sel_hi:[0,1,1]
	v_pk_fma_f32 v[198:199], v[208:209], v[76:77], v[44:45] op_sel_hi:[0,1,1]
	v_pk_fma_f32 v[196:197], v[190:191], v[206:207], v[196:197] op_sel_hi:[1,0,1]
	v_pk_fma_f32 v[198:199], v[192:193], v[206:207], v[198:199] op_sel_hi:[1,0,1]
	v_cvt_pk_f16_f32 v200, v196, v197
	v_cvt_pk_f16_f32 v201, v198, v199
	v_pk_max_f16 v200, v200, 0
	v_pk_max_f16 v201, v201, 0
	v_pk_fma_f32 v[196:197], v[208:209], v[78:79], v[50:51] op_sel_hi:[0,1,1]
	v_pk_fma_f32 v[198:199], v[208:209], v[80:81], v[52:53] op_sel_hi:[0,1,1]
	v_pk_fma_f32 v[196:197], v[186:187], v[206:207], v[196:197] op_sel_hi:[1,0,1]
	v_pk_fma_f32 v[198:199], v[188:189], v[206:207], v[198:199] op_sel_hi:[1,0,1]
	v_cvt_pk_f16_f32 v202, v196, v197
	v_cvt_pk_f16_f32 v203, v198, v199
	v_pk_max_f16 v202, v202, 0
	v_pk_max_f16 v203, v203, 0
	s_nop 1
	v_permlane16_swap_b32_e32 v200, v202
	v_permlane16_swap_b32_e32 v201, v203
	buffer_store_dwordx4 v[200:203], v210, s[12:15], 0 offen sc1
	v_pk_fma_f32 v[196:197], v[208:209], v[82:83], v[54:55] op_sel_hi:[0,1,1]
	v_pk_fma_f32 v[198:199], v[208:209], v[84:85], v[56:57] op_sel_hi:[0,1,1]
	v_pk_fma_f32 v[196:197], v[182:183], v[206:207], v[196:197] op_sel_hi:[1,0,1]
	v_pk_fma_f32 v[198:199], v[184:185], v[206:207], v[198:199] op_sel_hi:[1,0,1]
	v_cvt_pk_f16_f32 v200, v196, v197
	v_cvt_pk_f16_f32 v201, v198, v199
	v_pk_max_f16 v200, v200, 0
	v_pk_max_f16 v201, v201, 0
	v_pk_fma_f32 v[196:197], v[208:209], v[86:87], v[62:63] op_sel_hi:[0,1,1]
	v_pk_fma_f32 v[198:199], v[208:209], v[88:89], v[64:65] op_sel_hi:[0,1,1]
	v_pk_fma_f32 v[196:197], v[174:175], v[206:207], v[196:197] op_sel_hi:[1,0,1]
	v_pk_fma_f32 v[198:199], v[176:177], v[206:207], v[198:199] op_sel_hi:[1,0,1]
	v_cvt_pk_f16_f32 v202, v196, v197
	v_cvt_pk_f16_f32 v203, v198, v199
	v_pk_max_f16 v202, v202, 0
	v_pk_max_f16 v203, v203, 0
	s_nop 1
	v_permlane16_swap_b32_e32 v200, v202
	v_permlane16_swap_b32_e32 v201, v203
	buffer_store_dwordx4 v[200:203], v210, s[12:15], 0 offen offset:64 sc1
	v_pk_fma_f32 v[196:197], v[208:209], v[90:91], v[66:67] op_sel_hi:[0,1,1]
	v_pk_fma_f32 v[198:199], v[208:209], v[92:93], v[68:69] op_sel_hi:[0,1,1]
	v_pk_fma_f32 v[196:197], v[178:179], v[206:207], v[196:197] op_sel_hi:[1,0,1]
	v_pk_fma_f32 v[198:199], v[180:181], v[206:207], v[198:199] op_sel_hi:[1,0,1]
	v_cvt_pk_f16_f32 v200, v196, v197
	v_cvt_pk_f16_f32 v201, v198, v199
	v_pk_max_f16 v200, v200, 0
	v_pk_max_f16 v201, v201, 0
	v_pk_fma_f32 v[196:197], v[208:209], v[94:95], v[18:19] op_sel_hi:[0,1,1]
	v_pk_fma_f32 v[198:199], v[208:209], v[96:97], v[20:21] op_sel_hi:[0,1,1]
	v_pk_fma_f32 v[196:197], v[170:171], v[206:207], v[196:197] op_sel_hi:[1,0,1]
	v_pk_fma_f32 v[198:199], v[172:173], v[206:207], v[198:199] op_sel_hi:[1,0,1]
	v_cvt_pk_f16_f32 v202, v196, v197
	v_cvt_pk_f16_f32 v203, v198, v199
	v_pk_max_f16 v202, v202, 0
	v_pk_max_f16 v203, v203, 0
	s_nop 1
	v_permlane16_swap_b32_e32 v200, v202
	v_permlane16_swap_b32_e32 v201, v203
	buffer_store_dwordx4 v[200:203], v210, s[12:15], 0 offen offset:256 sc1
	v_pk_fma_f32 v[196:197], v[208:209], v[34:35], v[22:23] op_sel_hi:[0,1,1]
	v_pk_fma_f32 v[198:199], v[208:209], v[36:37], v[24:25] op_sel_hi:[0,1,1]
	v_pk_fma_f32 v[196:197], v[166:167], v[206:207], v[196:197] op_sel_hi:[1,0,1]
	v_pk_fma_f32 v[198:199], v[168:169], v[206:207], v[198:199] op_sel_hi:[1,0,1]
	v_cvt_pk_f16_f32 v200, v196, v197
	v_cvt_pk_f16_f32 v201, v198, v199
	v_pk_max_f16 v200, v200, 0
	v_pk_max_f16 v201, v201, 0
	v_pk_fma_f32 v[196:197], v[208:209], v[38:39], v[10:11] op_sel_hi:[0,1,1]
	v_pk_fma_f32 v[198:199], v[208:209], v[40:41], v[12:13] op_sel_hi:[0,1,1]
	v_pk_fma_f32 v[196:197], v[162:163], v[206:207], v[196:197] op_sel_hi:[1,0,1]
	v_pk_fma_f32 v[198:199], v[164:165], v[206:207], v[198:199] op_sel_hi:[1,0,1]
	v_cvt_pk_f16_f32 v202, v196, v197
	v_cvt_pk_f16_f32 v203, v198, v199
	v_pk_max_f16 v202, v202, 0
	v_pk_max_f16 v203, v203, 0
	s_nop 1
	v_permlane16_swap_b32_e32 v200, v202
	v_permlane16_swap_b32_e32 v201, v203
	buffer_store_dwordx4 v[200:203], v210, s[12:15], 0 offen offset:320 sc1
	ds_read_b128 v[204:207], v212 offset:512
	ds_read_b128 v[196:199], v212 offset:528
	v_add_u32_e32 v210, 65536, v194
	s_waitcnt lgkmcnt(0)
	v_add_f32_e32 v204, v204, v206
	v_add_f32_e32 v196, v196, v198
	v_add_f32_e32 v204, v204, v196
	v_add_f32_e32 v205, v205, v207
	v_add_f32_e32 v197, v197, v199
	v_add_f32_e32 v205, v205, v197
	v_mul_f32_e32 v204, s36, v204
	v_mul_f32_e32 v205, s36, v205
	v_fma_f32 v205, -v204, v204, v205
	v_max_f32_e32 v205, 0, v205
	v_add_f32_e32 v205, 0x3727c5ac, v205
	v_rsq_f32_e32 v206, v205
	s_nop 0
	v_mul_f32_e64 v208, v206, -v204
	v_pk_fma_f32 v[196:197], v[208:209], v[74:75], v[42:43] op_sel_hi:[0,1,1]
	v_pk_fma_f32 v[198:199], v[208:209], v[76:77], v[44:45] op_sel_hi:[0,1,1]
	v_pk_fma_f32 v[196:197], v[158:159], v[206:207], v[196:197] op_sel_hi:[1,0,1]
	v_pk_fma_f32 v[198:199], v[160:161], v[206:207], v[198:199] op_sel_hi:[1,0,1]
	v_cvt_pk_f16_f32 v200, v196, v197
	v_cvt_pk_f16_f32 v201, v198, v199
	v_pk_max_f16 v200, v200, 0
	v_pk_max_f16 v201, v201, 0
	v_pk_fma_f32 v[196:197], v[208:209], v[78:79], v[50:51] op_sel_hi:[0,1,1]
	v_pk_fma_f32 v[198:199], v[208:209], v[80:81], v[52:53] op_sel_hi:[0,1,1]
	v_pk_fma_f32 v[196:197], v[154:155], v[206:207], v[196:197] op_sel_hi:[1,0,1]
	v_pk_fma_f32 v[198:199], v[156:157], v[206:207], v[198:199] op_sel_hi:[1,0,1]
	v_cvt_pk_f16_f32 v202, v196, v197
	v_cvt_pk_f16_f32 v203, v198, v199
	v_pk_max_f16 v202, v202, 0
	v_pk_max_f16 v203, v203, 0
	s_nop 1
	v_permlane16_swap_b32_e32 v200, v202
	v_permlane16_swap_b32_e32 v201, v203
	buffer_store_dwordx4 v[200:203], v210, s[12:15], 0 offen sc1
	v_pk_fma_f32 v[196:197], v[208:209], v[82:83], v[54:55] op_sel_hi:[0,1,1]
	v_pk_fma_f32 v[198:199], v[208:209], v[84:85], v[56:57] op_sel_hi:[0,1,1]
	v_pk_fma_f32 v[196:197], v[150:151], v[206:207], v[196:197] op_sel_hi:[1,0,1]
	v_pk_fma_f32 v[198:199], v[152:153], v[206:207], v[198:199] op_sel_hi:[1,0,1]
	v_cvt_pk_f16_f32 v200, v196, v197
	v_cvt_pk_f16_f32 v201, v198, v199
	v_pk_max_f16 v200, v200, 0
	v_pk_max_f16 v201, v201, 0
	v_pk_fma_f32 v[196:197], v[208:209], v[86:87], v[62:63] op_sel_hi:[0,1,1]
	v_pk_fma_f32 v[198:199], v[208:209], v[88:89], v[64:65] op_sel_hi:[0,1,1]
	v_pk_fma_f32 v[196:197], v[142:143], v[206:207], v[196:197] op_sel_hi:[1,0,1]
	v_pk_fma_f32 v[198:199], v[144:145], v[206:207], v[198:199] op_sel_hi:[1,0,1]
	v_cvt_pk_f16_f32 v202, v196, v197
	v_cvt_pk_f16_f32 v203, v198, v199
	v_pk_max_f16 v202, v202, 0
	v_pk_max_f16 v203, v203, 0
	s_nop 1
	v_permlane16_swap_b32_e32 v200, v202
	v_permlane16_swap_b32_e32 v201, v203
	buffer_store_dwordx4 v[200:203], v210, s[12:15], 0 offen offset:64 sc1
	v_pk_fma_f32 v[196:197], v[208:209], v[90:91], v[66:67] op_sel_hi:[0,1,1]
	v_pk_fma_f32 v[198:199], v[208:209], v[92:93], v[68:69] op_sel_hi:[0,1,1]
	v_pk_fma_f32 v[196:197], v[146:147], v[206:207], v[196:197] op_sel_hi:[1,0,1]
	v_pk_fma_f32 v[198:199], v[148:149], v[206:207], v[198:199] op_sel_hi:[1,0,1]
	v_cvt_pk_f16_f32 v200, v196, v197
	v_cvt_pk_f16_f32 v201, v198, v199
	v_pk_max_f16 v200, v200, 0
	v_pk_max_f16 v201, v201, 0
	v_pk_fma_f32 v[196:197], v[208:209], v[94:95], v[18:19] op_sel_hi:[0,1,1]
	v_pk_fma_f32 v[198:199], v[208:209], v[96:97], v[20:21] op_sel_hi:[0,1,1]
	v_pk_fma_f32 v[196:197], v[138:139], v[206:207], v[196:197] op_sel_hi:[1,0,1]
	v_pk_fma_f32 v[198:199], v[140:141], v[206:207], v[198:199] op_sel_hi:[1,0,1]
	v_cvt_pk_f16_f32 v202, v196, v197
	v_cvt_pk_f16_f32 v203, v198, v199
	v_pk_max_f16 v202, v202, 0
	v_pk_max_f16 v203, v203, 0
	s_nop 1
	v_permlane16_swap_b32_e32 v200, v202
	v_permlane16_swap_b32_e32 v201, v203
	buffer_store_dwordx4 v[200:203], v210, s[12:15], 0 offen offset:256 sc1
	v_pk_fma_f32 v[196:197], v[208:209], v[34:35], v[22:23] op_sel_hi:[0,1,1]
	v_pk_fma_f32 v[198:199], v[208:209], v[36:37], v[24:25] op_sel_hi:[0,1,1]
	v_pk_fma_f32 v[196:197], v[134:135], v[206:207], v[196:197] op_sel_hi:[1,0,1]
	v_pk_fma_f32 v[198:199], v[136:137], v[206:207], v[198:199] op_sel_hi:[1,0,1]
	v_cvt_pk_f16_f32 v200, v196, v197
	v_cvt_pk_f16_f32 v201, v198, v199
	v_pk_max_f16 v200, v200, 0
	v_pk_max_f16 v201, v201, 0
	v_pk_fma_f32 v[196:197], v[208:209], v[38:39], v[10:11] op_sel_hi:[0,1,1]
	v_pk_fma_f32 v[198:199], v[208:209], v[40:41], v[12:13] op_sel_hi:[0,1,1]
	v_pk_fma_f32 v[196:197], v[130:131], v[206:207], v[196:197] op_sel_hi:[1,0,1]
	v_pk_fma_f32 v[198:199], v[132:133], v[206:207], v[198:199] op_sel_hi:[1,0,1]
	v_cvt_pk_f16_f32 v202, v196, v197
	v_cvt_pk_f16_f32 v203, v198, v199
	v_pk_max_f16 v202, v202, 0
	v_pk_max_f16 v203, v203, 0
	s_nop 1
	v_permlane16_swap_b32_e32 v200, v202
	v_permlane16_swap_b32_e32 v201, v203
	buffer_store_dwordx4 v[200:203], v210, s[12:15], 0 offen offset:320 sc1
	ds_read_b128 v[204:207], v212 offset:4096
	ds_read_b128 v[196:199], v212 offset:4112
	v_add_u32_e32 v210, 524288, v194
	s_waitcnt lgkmcnt(0)
	v_add_f32_e32 v204, v204, v206
	v_add_f32_e32 v196, v196, v198
	v_add_f32_e32 v204, v204, v196
	v_add_f32_e32 v205, v205, v207
	v_add_f32_e32 v197, v197, v199
	v_add_f32_e32 v205, v205, v197
	v_mul_f32_e32 v204, s36, v204
	v_mul_f32_e32 v205, s36, v205
	v_fma_f32 v205, -v204, v204, v205
	v_max_f32_e32 v205, 0, v205
	v_add_f32_e32 v205, 0x3727c5ac, v205
	v_rsq_f32_e32 v206, v205
	s_nop 0
	v_mul_f32_e64 v208, v206, -v204
	v_pk_fma_f32 v[196:197], v[208:209], v[74:75], v[42:43] op_sel_hi:[0,1,1]
	v_pk_fma_f32 v[198:199], v[208:209], v[76:77], v[44:45] op_sel_hi:[0,1,1]
	v_pk_fma_f32 v[196:197], v[126:127], v[206:207], v[196:197] op_sel_hi:[1,0,1]
	v_pk_fma_f32 v[198:199], v[128:129], v[206:207], v[198:199] op_sel_hi:[1,0,1]
	v_cvt_pk_f16_f32 v200, v196, v197
	v_cvt_pk_f16_f32 v201, v198, v199
	v_pk_max_f16 v200, v200, 0
	v_pk_max_f16 v201, v201, 0
	v_pk_fma_f32 v[196:197], v[208:209], v[78:79], v[50:51] op_sel_hi:[0,1,1]
	v_pk_fma_f32 v[198:199], v[208:209], v[80:81], v[52:53] op_sel_hi:[0,1,1]
	v_pk_fma_f32 v[196:197], v[122:123], v[206:207], v[196:197] op_sel_hi:[1,0,1]
	v_pk_fma_f32 v[198:199], v[124:125], v[206:207], v[198:199] op_sel_hi:[1,0,1]
	v_cvt_pk_f16_f32 v202, v196, v197
	v_cvt_pk_f16_f32 v203, v198, v199
	v_pk_max_f16 v202, v202, 0
	v_pk_max_f16 v203, v203, 0
	s_nop 1
	v_permlane16_swap_b32_e32 v200, v202
	v_permlane16_swap_b32_e32 v201, v203
	buffer_store_dwordx4 v[200:203], v210, s[12:15], 0 offen sc1
	v_pk_fma_f32 v[196:197], v[208:209], v[82:83], v[54:55] op_sel_hi:[0,1,1]
	v_pk_fma_f32 v[198:199], v[208:209], v[84:85], v[56:57] op_sel_hi:[0,1,1]
	v_pk_fma_f32 v[196:197], v[118:119], v[206:207], v[196:197] op_sel_hi:[1,0,1]
	v_pk_fma_f32 v[198:199], v[120:121], v[206:207], v[198:199] op_sel_hi:[1,0,1]
	v_cvt_pk_f16_f32 v200, v196, v197
	v_cvt_pk_f16_f32 v201, v198, v199
	v_pk_max_f16 v200, v200, 0
	v_pk_max_f16 v201, v201, 0
	v_pk_fma_f32 v[196:197], v[208:209], v[86:87], v[62:63] op_sel_hi:[0,1,1]
	v_pk_fma_f32 v[198:199], v[208:209], v[88:89], v[64:65] op_sel_hi:[0,1,1]
	v_pk_fma_f32 v[196:197], v[114:115], v[206:207], v[196:197] op_sel_hi:[1,0,1]
	v_pk_fma_f32 v[198:199], v[116:117], v[206:207], v[198:199] op_sel_hi:[1,0,1]
	v_cvt_pk_f16_f32 v202, v196, v197
	v_cvt_pk_f16_f32 v203, v198, v199
	v_pk_max_f16 v202, v202, 0
	v_pk_max_f16 v203, v203, 0
	s_nop 1
	v_permlane16_swap_b32_e32 v200, v202
	v_permlane16_swap_b32_e32 v201, v203
	buffer_store_dwordx4 v[200:203], v210, s[12:15], 0 offen offset:64 sc1
	v_pk_fma_f32 v[196:197], v[208:209], v[90:91], v[66:67] op_sel_hi:[0,1,1]
	v_pk_fma_f32 v[198:199], v[208:209], v[92:93], v[68:69] op_sel_hi:[0,1,1]
	v_pk_fma_f32 v[196:197], v[110:111], v[206:207], v[196:197] op_sel_hi:[1,0,1]
	v_pk_fma_f32 v[198:199], v[112:113], v[206:207], v[198:199] op_sel_hi:[1,0,1]
	v_cvt_pk_f16_f32 v200, v196, v197
	v_cvt_pk_f16_f32 v201, v198, v199
	v_pk_max_f16 v200, v200, 0
	v_pk_max_f16 v201, v201, 0
	v_pk_fma_f32 v[196:197], v[208:209], v[94:95], v[18:19] op_sel_hi:[0,1,1]
	v_pk_fma_f32 v[198:199], v[208:209], v[96:97], v[20:21] op_sel_hi:[0,1,1]
	v_pk_fma_f32 v[196:197], v[106:107], v[206:207], v[196:197] op_sel_hi:[1,0,1]
	v_pk_fma_f32 v[198:199], v[108:109], v[206:207], v[198:199] op_sel_hi:[1,0,1]
	v_cvt_pk_f16_f32 v202, v196, v197
	v_cvt_pk_f16_f32 v203, v198, v199
	v_pk_max_f16 v202, v202, 0
	v_pk_max_f16 v203, v203, 0
	s_nop 1
	v_permlane16_swap_b32_e32 v200, v202
	v_permlane16_swap_b32_e32 v201, v203
	buffer_store_dwordx4 v[200:203], v210, s[12:15], 0 offen offset:256 sc1
	v_pk_fma_f32 v[196:197], v[208:209], v[34:35], v[22:23] op_sel_hi:[0,1,1]
	v_pk_fma_f32 v[198:199], v[208:209], v[36:37], v[24:25] op_sel_hi:[0,1,1]
	v_pk_fma_f32 v[196:197], v[102:103], v[206:207], v[196:197] op_sel_hi:[1,0,1]
	v_pk_fma_f32 v[198:199], v[104:105], v[206:207], v[198:199] op_sel_hi:[1,0,1]
	v_cvt_pk_f16_f32 v200, v196, v197
	v_cvt_pk_f16_f32 v201, v198, v199
	v_pk_max_f16 v200, v200, 0
	v_pk_max_f16 v201, v201, 0
	v_pk_fma_f32 v[196:197], v[208:209], v[38:39], v[10:11] op_sel_hi:[0,1,1]
	v_pk_fma_f32 v[198:199], v[208:209], v[40:41], v[12:13] op_sel_hi:[0,1,1]
	v_pk_fma_f32 v[196:197], v[98:99], v[206:207], v[196:197] op_sel_hi:[1,0,1]
	v_pk_fma_f32 v[198:199], v[100:101], v[206:207], v[198:199] op_sel_hi:[1,0,1]
	v_cvt_pk_f16_f32 v202, v196, v197
	v_cvt_pk_f16_f32 v203, v198, v199
	v_pk_max_f16 v202, v202, 0
	v_pk_max_f16 v203, v203, 0
	s_nop 1
	v_permlane16_swap_b32_e32 v200, v202
	v_permlane16_swap_b32_e32 v201, v203
	buffer_store_dwordx4 v[200:203], v210, s[12:15], 0 offen offset:320 sc1
	ds_read_b128 v[204:207], v212 offset:4608
	ds_read_b128 v[196:199], v212 offset:4624
	v_add_u32_e32 v210, 589824, v194
	s_waitcnt lgkmcnt(0)
	v_add_f32_e32 v204, v204, v206
	v_add_f32_e32 v196, v196, v198
	v_add_f32_e32 v204, v204, v196
	v_add_f32_e32 v205, v205, v207
	v_add_f32_e32 v197, v197, v199
	v_add_f32_e32 v205, v205, v197
	v_mul_f32_e32 v204, s36, v204
	v_mul_f32_e32 v205, s36, v205
	v_fma_f32 v205, -v204, v204, v205
	v_max_f32_e32 v205, 0, v205
	v_add_f32_e32 v205, 0x3727c5ac, v205
	v_rsq_f32_e32 v206, v205
	s_nop 0
	v_mul_f32_e64 v208, v206, -v204
	v_pk_fma_f32 v[196:197], v[208:209], v[74:75], v[42:43] op_sel_hi:[0,1,1]
	v_pk_fma_f32 v[198:199], v[208:209], v[76:77], v[44:45] op_sel_hi:[0,1,1]
	v_pk_fma_f32 v[196:197], v[70:71], v[206:207], v[196:197] op_sel_hi:[1,0,1]
	v_pk_fma_f32 v[198:199], v[72:73], v[206:207], v[198:199] op_sel_hi:[1,0,1]
	v_cvt_pk_f16_f32 v200, v196, v197
	v_cvt_pk_f16_f32 v201, v198, v199
	v_pk_max_f16 v200, v200, 0
	v_pk_max_f16 v201, v201, 0
	v_pk_fma_f32 v[196:197], v[208:209], v[78:79], v[50:51] op_sel_hi:[0,1,1]
	v_pk_fma_f32 v[198:199], v[208:209], v[80:81], v[52:53] op_sel_hi:[0,1,1]
	v_pk_fma_f32 v[196:197], v[58:59], v[206:207], v[196:197] op_sel_hi:[1,0,1]
	v_pk_fma_f32 v[198:199], v[60:61], v[206:207], v[198:199] op_sel_hi:[1,0,1]
	v_cvt_pk_f16_f32 v202, v196, v197
	v_cvt_pk_f16_f32 v203, v198, v199
	v_pk_max_f16 v202, v202, 0
	v_pk_max_f16 v203, v203, 0
	s_nop 1
	v_permlane16_swap_b32_e32 v200, v202
	v_permlane16_swap_b32_e32 v201, v203
	buffer_store_dwordx4 v[200:203], v210, s[12:15], 0 offen sc1
	v_pk_fma_f32 v[196:197], v[208:209], v[82:83], v[54:55] op_sel_hi:[0,1,1]
	v_pk_fma_f32 v[198:199], v[208:209], v[84:85], v[56:57] op_sel_hi:[0,1,1]
	v_pk_fma_f32 v[196:197], v[46:47], v[206:207], v[196:197] op_sel_hi:[1,0,1]
	v_pk_fma_f32 v[198:199], v[48:49], v[206:207], v[198:199] op_sel_hi:[1,0,1]
	v_cvt_pk_f16_f32 v200, v196, v197
	v_cvt_pk_f16_f32 v201, v198, v199
	v_pk_max_f16 v200, v200, 0
	v_pk_max_f16 v201, v201, 0
	v_pk_fma_f32 v[196:197], v[208:209], v[86:87], v[62:63] op_sel_hi:[0,1,1]
	v_pk_fma_f32 v[198:199], v[208:209], v[88:89], v[64:65] op_sel_hi:[0,1,1]
	v_pk_fma_f32 v[196:197], v[30:31], v[206:207], v[196:197] op_sel_hi:[1,0,1]
	v_pk_fma_f32 v[198:199], v[32:33], v[206:207], v[198:199] op_sel_hi:[1,0,1]
	v_cvt_pk_f16_f32 v202, v196, v197
	v_cvt_pk_f16_f32 v203, v198, v199
	v_pk_max_f16 v202, v202, 0
	v_pk_max_f16 v203, v203, 0
	s_nop 1
	v_permlane16_swap_b32_e32 v200, v202
	v_permlane16_swap_b32_e32 v201, v203
	buffer_store_dwordx4 v[200:203], v210, s[12:15], 0 offen offset:64 sc1
	v_pk_fma_f32 v[196:197], v[208:209], v[90:91], v[66:67] op_sel_hi:[0,1,1]
	v_pk_fma_f32 v[198:199], v[208:209], v[92:93], v[68:69] op_sel_hi:[0,1,1]
	v_pk_fma_f32 v[196:197], v[26:27], v[206:207], v[196:197] op_sel_hi:[1,0,1]
	v_pk_fma_f32 v[198:199], v[28:29], v[206:207], v[198:199] op_sel_hi:[1,0,1]
	v_cvt_pk_f16_f32 v200, v196, v197
	v_cvt_pk_f16_f32 v201, v198, v199
	v_pk_max_f16 v200, v200, 0
	v_pk_max_f16 v201, v201, 0
	v_pk_fma_f32 v[196:197], v[208:209], v[94:95], v[18:19] op_sel_hi:[0,1,1]
	v_pk_fma_f32 v[198:199], v[208:209], v[96:97], v[20:21] op_sel_hi:[0,1,1]
	v_pk_fma_f32 v[196:197], v[14:15], v[206:207], v[196:197] op_sel_hi:[1,0,1]
	v_pk_fma_f32 v[198:199], v[16:17], v[206:207], v[198:199] op_sel_hi:[1,0,1]
	v_cvt_pk_f16_f32 v202, v196, v197
	v_cvt_pk_f16_f32 v203, v198, v199
	v_pk_max_f16 v202, v202, 0
	v_pk_max_f16 v203, v203, 0
	s_nop 1
	v_permlane16_swap_b32_e32 v200, v202
	v_permlane16_swap_b32_e32 v201, v203
	buffer_store_dwordx4 v[200:203], v210, s[12:15], 0 offen offset:256 sc1
	v_pk_fma_f32 v[196:197], v[208:209], v[34:35], v[22:23] op_sel_hi:[0,1,1]
	v_pk_fma_f32 v[198:199], v[208:209], v[36:37], v[24:25] op_sel_hi:[0,1,1]
	v_pk_fma_f32 v[196:197], v[6:7], v[206:207], v[196:197] op_sel_hi:[1,0,1]
	v_pk_fma_f32 v[198:199], v[8:9], v[206:207], v[198:199] op_sel_hi:[1,0,1]
	v_cvt_pk_f16_f32 v200, v196, v197
	v_cvt_pk_f16_f32 v201, v198, v199
	v_pk_max_f16 v200, v200, 0
	v_pk_max_f16 v201, v201, 0
	v_pk_fma_f32 v[196:197], v[208:209], v[38:39], v[10:11] op_sel_hi:[0,1,1]
	v_pk_fma_f32 v[198:199], v[208:209], v[40:41], v[12:13] op_sel_hi:[0,1,1]
	v_pk_fma_f32 v[196:197], v[2:3], v[206:207], v[196:197] op_sel_hi:[1,0,1]
	v_pk_fma_f32 v[198:199], v[4:5], v[206:207], v[198:199] op_sel_hi:[1,0,1]
	v_cvt_pk_f16_f32 v202, v196, v197
	v_cvt_pk_f16_f32 v203, v198, v199
	v_pk_max_f16 v202, v202, 0
	v_pk_max_f16 v203, v203, 0
	s_nop 1
	v_permlane16_swap_b32_e32 v200, v202
	v_permlane16_swap_b32_e32 v201, v203
	buffer_store_dwordx4 v[200:203], v210, s[12:15], 0 offen offset:320 sc1
	s_add_i32 s2, s2, s8
	s_xor_b32 s33, s33, 1
	s_cmp_ge_i32 s2, s3
	s_cbranch_scc1 .LBB9_41

	.amdhsa_kernel _Z14gemm256_kernelILi2ELi512ELi2048EEv8GemmArgs
		.amdhsa_group_segment_fixed_size 0
		.amdhsa_private_segment_fixed_size 0
		.amdhsa_kernarg_size 592
		.amdhsa_user_sgpr_count 2
		.amdhsa_user_sgpr_dispatch_ptr 0
		.amdhsa_user_sgpr_queue_ptr 0
		.amdhsa_user_sgpr_kernarg_segment_ptr 1
		.amdhsa_user_sgpr_dispatch_id 0
		.amdhsa_user_sgpr_kernarg_preload_length 0
		.amdhsa_user_sgpr_kernarg_preload_offset 0
		.amdhsa_user_sgpr_private_segment_size 0
		.amdhsa_uses_dynamic_stack 0
		.amdhsa_enable_private_segment 0
		.amdhsa_system_sgpr_workgroup_id_x 1
		.amdhsa_system_sgpr_workgroup_id_y 0
		.amdhsa_system_sgpr_workgroup_id_z 0
		.amdhsa_system_sgpr_workgroup_info 0
		.amdhsa_system_vgpr_workitem_id 0
		.amdhsa_next_free_vgpr 254
		.amdhsa_next_free_sgpr 65
		.amdhsa_accum_offset 256
		.amdhsa_reserve_vcc 1
		.amdhsa_float_round_mode_32 0
		.amdhsa_float_round_mode_16_64 0
		.amdhsa_float_denorm_mode_32 3
		.amdhsa_float_denorm_mode_16_64 3
		.amdhsa_dx10_clamp 1
		.amdhsa_ieee_mode 1
		.amdhsa_fp16_overflow 0
		.amdhsa_tg_split 0
		.amdhsa_exception_fp_ieee_invalid_op 0
		.amdhsa_exception_fp_denorm_src 0
		.amdhsa_exception_fp_ieee_div_zero 0
		.amdhsa_exception_fp_ieee_overflow 0
		.amdhsa_exception_fp_ieee_underflow 0
		.amdhsa_exception_fp_ieee_inexact 0
		.amdhsa_exception_int_div_zero 0
	.end_amdhsa_kernel

amdhsa.kernels:
  - .agpr_count:     0
    .args:
      - .offset:         0
        .size:           136
        .value_kind:     by_value
      - .actual_access:  read_only
        .address_space:  global
        .offset:         136
        .size:           8
        .value_kind:     global_buffer
      - .actual_access:  read_only
        .address_space:  global
        .offset:         144
        .size:           8
        .value_kind:     global_buffer
      - .actual_access:  read_only
        .address_space:  global
        .offset:         152
        .size:           8
        .value_kind:     global_buffer
      - .actual_access:  read_only
        .address_space:  global
        .offset:         160
        .size:           8
        .value_kind:     global_buffer
      - .actual_access:  write_only
        .address_space:  global
        .offset:         168
        .size:           8
        .value_kind:     global_buffer
      - .actual_access:  write_only
        .address_space:  global
        .offset:         176
        .size:           8
        .value_kind:     global_buffer
    .group_segment_fixed_size: 0
    .kernarg_segment_align: 8
    .kernarg_segment_size: 184
    .language:       OpenCL C
    .language_version:
      - 2
      - 0
    .max_flat_workgroup_size: 256
    .name:           _Z15prologue_kernel8PrepArgsPKfS1_PKiS1_PDF16_Pf
    .private_segment_fixed_size: 0
    .sgpr_count:     36
    .sgpr_spill_count: 0
    .symbol:         _Z15prologue_kernel8PrepArgsPKfS1_PKiS1_PDF16_Pf.kd
    .uniform_work_group_size: 1
    .uses_dynamic_stack: false
    .vgpr_count:     44
    .vgpr_spill_count: 0
    .wavefront_size: 64
  - .agpr_count:     0
    .args:
      - .actual_access:  read_only
        .address_space:  global
        .offset:         0
        .size:           8
        .value_kind:     global_buffer
      - .offset:         8
        .size:           4
        .value_kind:     by_value
      - .offset:         12
        .size:           4
        .value_kind:     by_value
      - .actual_access:  read_only
        .address_space:  global
        .offset:         16
        .size:           8
        .value_kind:     global_buffer
      - .actual_access:  read_only
        .address_space:  global
        .offset:         24
        .size:           8
        .value_kind:     global_buffer
      - .actual_access:  read_only
        .address_space:  global
        .offset:         32
        .size:           8
        .value_kind:     global_buffer
      - .actual_access:  read_only
        .address_space:  global
        .offset:         40
        .size:           8
        .value_kind:     global_buffer
      - .address_space:  global
        .offset:         48
        .size:           8
        .value_kind:     global_buffer
      - .actual_access:  write_only
        .address_space:  global
        .offset:         56
        .size:           8
        .value_kind:     global_buffer
    .group_segment_fixed_size: 0
    .kernarg_segment_align: 8
    .kernarg_segment_size: 64
    .language:       OpenCL C
    .language_version:
      - 2
      - 0
    .max_flat_workgroup_size: 256
    .name:           _Z18ffn2_finish_kernelPKfiiS0_PK15HIP_vector_typeIfLj2EES0_S0_PDF16_PS2_
    .private_segment_fixed_size: 0
    .sgpr_count:     20
    .sgpr_spill_count: 0
    .symbol:         _Z18ffn2_finish_kernelPKfiiS0_PK15HIP_vector_typeIfLj2EES0_S0_PDF16_PS2_.kd
    .uniform_work_group_size: 1
    .uses_dynamic_stack: false
    .vgpr_count:     52
    .vgpr_spill_count: 0
    .wavefront_size: 64
  - .agpr_count:     0
    .args:
      - .actual_access:  read_only
        .address_space:  global
        .offset:         0
        .size:           8
        .value_kind:     global_buffer
      - .actual_access:  read_only
        .address_space:  global
        .offset:         8
        .size:           8
        .value_kind:     global_buffer
      - .actual_access:  read_only
        .address_space:  global
        .offset:         16
        .size:           8
        .value_kind:     global_buffer
      - .actual_access:  write_only
        .address_space:  global
        .offset:         24
        .size:           8
        .value_kind:     global_buffer
      - .offset:         32
        .size:           4
        .value_kind:     by_value
    .group_segment_fixed_size: 0
    .kernarg_segment_align: 8
    .kernarg_segment_size: 36
    .language:       OpenCL C
    .language_version:
      - 2
      - 0
    .max_flat_workgroup_size: 1024
    .name:           _Z14attn_bh_kernelPKDF16_S0_S0_PDF16_i
    .private_segment_fixed_size: 0
    .sgpr_count:     38
    .sgpr_spill_count: 0
    .symbol:         _Z14attn_bh_kernelPKDF16_S0_S0_PDF16_i.kd
    .uniform_work_group_size: 1
    .uses_dynamic_stack: false
    .vgpr_count:     120
    .vgpr_spill_count: 0
    .wavefront_size: 64
  - .agpr_count:     0
    .args:
      - .offset:         0
        .size:           336
        .value_kind:     by_value
    .group_segment_fixed_size: 0
    .kernarg_segment_align: 8
    .kernarg_segment_size: 336
    .language:       OpenCL C
    .language_version:
      - 2
      - 0
    .max_flat_workgroup_size: 256
    .name:           _Z11gemm_kernelILi0EEv8GemmArgs
    .private_segment_fixed_size: 0
    .sgpr_count:     47
    .sgpr_spill_count: 0
    .symbol:         _Z11gemm_kernelILi0EEv8GemmArgs.kd
    .uniform_work_group_size: 1
    .uses_dynamic_stack: false
    .vgpr_count:     198
    .vgpr_spill_count: 0
    .wavefront_size: 64
  - .agpr_count:     0
    .args:
      - .offset:         0
        .size:           336
        .value_kind:     by_value
    .group_segment_fixed_size: 0
    .kernarg_segment_align: 8
    .kernarg_segment_size: 336
    .language:       OpenCL C
    .language_version:
      - 2
      - 0
    .max_flat_workgroup_size: 256
    .name:           _Z11gemm_kernelILi1EEv8GemmArgs
    .private_segment_fixed_size: 0
    .sgpr_count:     43
    .sgpr_spill_count: 0
    .symbol:         _Z11gemm_kernelILi1EEv8GemmArgs.kd
    .uniform_work_group_size: 1
    .uses_dynamic_stack: false
    .vgpr_count:     202
    .vgpr_spill_count: 0
    .wavefront_size: 64
  - .agpr_count:     0
    .args:
      - .offset:         0
        .size:           336
        .value_kind:     by_value
    .group_segment_fixed_size: 0
    .kernarg_segment_align: 8
    .kernarg_segment_size: 336
    .language:       OpenCL C
    .language_version:
      - 2
      - 0
    .max_flat_workgroup_size: 256
    .name:           _Z11gemm_kernelILi2EEv8GemmArgs
    .private_segment_fixed_size: 0
    .sgpr_count:     41
    .sgpr_spill_count: 0
    .symbol:         _Z11gemm_kernelILi2EEv8GemmArgs.kd
    .uniform_work_group_size: 1
    .uses_dynamic_stack: false
    .vgpr_count:     198
    .vgpr_spill_count: 0
    .wavefront_size: 64
  - .agpr_count:     0
    .args:
      - .offset:         0
        .size:           336
        .value_kind:     by_value
      - .offset:         336
        .size:           4
        .value_kind:     hidden_block_count_x
      - .offset:         340
        .size:           4
        .value_kind:     hidden_block_count_y
      - .offset:         344
        .size:           4
        .value_kind:     hidden_block_count_z
      - .offset:         348
        .size:           2
        .value_kind:     hidden_group_size_x
      - .offset:         350
        .size:           2
        .value_kind:     hidden_group_size_y
      - .offset:         352
        .size:           2
        .value_kind:     hidden_group_size_z
      - .offset:         354
        .size:           2
        .value_kind:     hidden_remainder_x
      - .offset:         356
        .size:           2
        .value_kind:     hidden_remainder_y
      - .offset:         358
        .size:           2
        .value_kind:     hidden_remainder_z
      - .offset:         376
        .size:           8
        .value_kind:     hidden_global_offset_x
      - .offset:         384
        .size:           8
        .value_kind:     hidden_global_offset_y
      - .offset:         392
        .size:           8
        .value_kind:     hidden_global_offset_z
      - .offset:         400
        .size:           2
        .value_kind:     hidden_grid_dims
      - .offset:         456
        .size:           4
        .value_kind:     hidden_dynamic_lds_size
    .group_segment_fixed_size: 0
    .kernarg_segment_align: 8
    .kernarg_segment_size: 592
    .language:       OpenCL C
    .language_version:
      - 2
      - 0
    .max_flat_workgroup_size: 512
    .name:           _Z14gemm256_kernelILi0ELi512ELi1536EEv8GemmArgs
    .private_segment_fixed_size: 0
    .sgpr_count:     78
    .sgpr_spill_count: 0
    .symbol:         _Z14gemm256_kernelILi0ELi512ELi1536EEv8GemmArgs.kd
    .uniform_work_group_size: 1
    .uses_dynamic_stack: false
    .vgpr_count:     256
    .vgpr_spill_count: 0
    .wavefront_size: 64
  - .agpr_count:     0
    .args:
      - .offset:         0
        .size:           336
        .value_kind:     by_value
      - .offset:         336
        .size:           4
        .value_kind:     hidden_block_count_x
      - .offset:         340
        .size:           4
        .value_kind:     hidden_block_count_y
      - .offset:         344
        .size:           4
        .value_kind:     hidden_block_count_z
      - .offset:         348
        .size:           2
        .value_kind:     hidden_group_size_x
      - .offset:         350
        .size:           2
        .value_kind:     hidden_group_size_y
      - .offset:         352
        .size:           2
        .value_kind:     hidden_group_size_z
      - .offset:         354
        .size:           2
        .value_kind:     hidden_remainder_x
      - .offset:         356
        .size:           2
        .value_kind:     hidden_remainder_y
      - .offset:         358
        .size:           2
        .value_kind:     hidden_remainder_z
      - .offset:         376
        .size:           8
        .value_kind:     hidden_global_offset_x
      - .offset:         384
        .size:           8
        .value_kind:     hidden_global_offset_y
      - .offset:         392
        .size:           8
        .value_kind:     hidden_global_offset_z
      - .offset:         400
        .size:           2
        .value_kind:     hidden_grid_dims
      - .offset:         456
        .size:           4
        .value_kind:     hidden_dynamic_lds_size
    .group_segment_fixed_size: 0
    .kernarg_segment_align: 8
    .kernarg_segment_size: 592
    .language:       OpenCL C
    .language_version:
      - 2
      - 0
    .max_flat_workgroup_size: 512
    .name:           _Z14gemm256_kernelILi0ELi512ELi1024EEv8GemmArgs
    .private_segment_fixed_size: 0
    .sgpr_count:     78
    .sgpr_spill_count: 0
    .symbol:         _Z14gemm256_kernelILi0ELi512ELi1024EEv8GemmArgs.kd
    .uniform_work_group_size: 1
    .uses_dynamic_stack: false
    .vgpr_count:     256
    .vgpr_spill_count: 0
    .wavefront_size: 64
  - .agpr_count:     0
    .args:
      - .offset:         0
        .size:           336
        .value_kind:     by_value
      - .offset:         336
        .size:           4
        .value_kind:     hidden_block_count_x
      - .offset:         340
        .size:           4
        .value_kind:     hidden_block_count_y
      - .offset:         344
        .size:           4
        .value_kind:     hidden_block_count_z
      - .offset:         348
        .size:           2
        .value_kind:     hidden_group_size_x
      - .offset:         350
        .size:           2
        .value_kind:     hidden_group_size_y
      - .offset:         352
        .size:           2
        .value_kind:     hidden_group_size_z
      - .offset:         354
        .size:           2
        .value_kind:     hidden_remainder_x
      - .offset:         356
        .size:           2
        .value_kind:     hidden_remainder_y
      - .offset:         358
        .size:           2
        .value_kind:     hidden_remainder_z
      - .offset:         376
        .size:           8
        .value_kind:     hidden_global_offset_x
      - .offset:         384
        .size:           8
        .value_kind:     hidden_global_offset_y
      - .offset:         392
        .size:           8
        .value_kind:     hidden_global_offset_z
      - .offset:         400
        .size:           2
        .value_kind:     hidden_grid_dims
      - .offset:         456
        .size:           4
        .value_kind:     hidden_dynamic_lds_size
    .group_segment_fixed_size: 0
    .kernarg_segment_align: 8
    .kernarg_segment_size: 592
    .language:       OpenCL C
    .language_version:
      - 2
      - 0
    .max_flat_workgroup_size: 512
    .name:           _Z14gemm256_kernelILi1ELi512ELi512EEv8GemmArgs
    .private_segment_fixed_size: 0
    .sgpr_count:     81
    .sgpr_spill_count: 0
    .symbol:         _Z14gemm256_kernelILi1ELi512ELi512EEv8GemmArgs.kd
    .uniform_work_group_size: 1
    .uses_dynamic_stack: false
    .vgpr_count:     256
    .vgpr_spill_count: 0
    .wavefront_size: 64
  - .agpr_count:     0
    .args:
      - .offset:         0
        .size:           336
        .value_kind:     by_value
      - .offset:         336
        .size:           4
        .value_kind:     hidden_block_count_x
      - .offset:         340
        .size:           4
        .value_kind:     hidden_block_count_y
      - .offset:         344
        .size:           4
        .value_kind:     hidden_block_count_z
      - .offset:         348
        .size:           2
        .value_kind:     hidden_group_size_x
      - .offset:         350
        .size:           2
        .value_kind:     hidden_group_size_y
      - .offset:         352
        .size:           2
        .value_kind:     hidden_group_size_z
      - .offset:         354
        .size:           2
        .value_kind:     hidden_remainder_x
      - .offset:         356
        .size:           2
        .value_kind:     hidden_remainder_y
      - .offset:         358
        .size:           2
        .value_kind:     hidden_remainder_z
      - .offset:         376
        .size:           8
        .value_kind:     hidden_global_offset_x
      - .offset:         384
        .size:           8
        .value_kind:     hidden_global_offset_y
      - .offset:         392
        .size:           8
        .value_kind:     hidden_global_offset_z
      - .offset:         400
        .size:           2
        .value_kind:     hidden_grid_dims
      - .offset:         456
        .size:           4
        .value_kind:     hidden_dynamic_lds_size
    .group_segment_fixed_size: 0
    .kernarg_segment_align: 8
    .kernarg_segment_size: 592
    .language:       OpenCL C
    .language_version:
      - 2
      - 0
    .max_flat_workgroup_size: 512
    .name:           _Z14gemm256_kernelILi2ELi512ELi2048EEv8GemmArgs
    .private_segment_fixed_size: 0
    .sgpr_count:     71
    .sgpr_spill_count: 0
    .symbol:         _Z14gemm256_kernelILi2ELi512ELi2048EEv8GemmArgs.kd
    .uniform_work_group_size: 1
    .uses_dynamic_stack: false
    .vgpr_count:     254
    .vgpr_spill_count: 0
    .wavefront_size: 64
  - .agpr_count:     0
    .args:
      - .offset:         0
        .size:           336
        .value_kind:     by_value
      - .offset:         336
        .size:           4
        .value_kind:     hidden_block_count_x
      - .offset:         340
        .size:           4
        .value_kind:     hidden_block_count_y
      - .offset:         344
        .size:           4
        .value_kind:     hidden_block_count_z
      - .offset:         348
        .size:           2
        .value_kind:     hidden_group_size_x
      - .offset:         350
        .size:           2
        .value_kind:     hidden_group_size_y
      - .offset:         352
        .size:           2
        .value_kind:     hidden_group_size_z
      - .offset:         354
        .size:           2
        .value_kind:     hidden_remainder_x
      - .offset:         356
        .size:           2
        .value_kind:     hidden_remainder_y
      - .offset:         358
        .size:           2
        .value_kind:     hidden_remainder_z
      - .offset:         376
        .size:           8
        .value_kind:     hidden_global_offset_x
      - .offset:         384
        .size:           8
        .value_kind:     hidden_global_offset_y
      - .offset:         392
        .size:           8
        .value_kind:     hidden_global_offset_z
      - .offset:         400
        .size:           2
        .value_kind:     hidden_grid_dims
      - .offset:         456
        .size:           4
        .value_kind:     hidden_dynamic_lds_size
    .group_segment_fixed_size: 0
    .kernarg_segment_align: 8
    .kernarg_segment_size: 592
    .language:       OpenCL C
    .language_version:
      - 2
      - 0
    .max_flat_workgroup_size: 512
    .name:           _Z14gemm256_kernelILi1ELi2048ELi512EEv8GemmArgs
    .private_segment_fixed_size: 0
    .sgpr_count:     76
    .sgpr_spill_count: 0
    .symbol:         _Z14gemm256_kernelILi1ELi2048ELi512EEv8GemmArgs.kd
    .uniform_work_group_size: 1
    .uses_dynamic_stack: false
    .vgpr_count:     256
    .vgpr_spill_count: 0
    .wavefront_size: 64
  - .agpr_count:     0
    .args:
      - .offset:         0
        .size:           336
        .value_kind:     by_value
    .group_segment_fixed_size: 0
    .kernarg_segment_align: 8
    .kernarg_segment_size: 336
    .language:       OpenCL C
    .language_version:
      - 2
      - 0
    .max_flat_workgroup_size: 256
    .name:           _Z11gemm_kernelILi4EEv8GemmArgs
    .private_segment_fixed_size: 0
    .sgpr_count:     42
    .sgpr_spill_count: 0
    .symbol:         _Z11gemm_kernelILi4EEv8GemmArgs.kd
    .uniform_work_group_size: 1
    .uses_dynamic_stack: false
    .vgpr_count:     196
    .vgpr_spill_count: 0
    .wavefront_size: 64
  - .agpr_count:     0
    .args:
      - .offset:         0
        .size:           336
        .value_kind:     by_value
    .group_segment_fixed_size: 0
    .kernarg_segment_align: 8
    .kernarg_segment_size: 336
    .language:       OpenCL C
    .language_version:
      - 2
      - 0
    .max_flat_workgroup_size: 256
    .name:           _Z11gemm_kernelILi3EEv8GemmArgs
    .private_segment_fixed_size: 0
    .sgpr_count:     38
    .sgpr_spill_count: 0
    .symbol:         _Z11gemm_kernelILi3EEv8GemmArgs.kd
    .uniform_work_group_size: 1
    .uses_dynamic_stack: false
    .vgpr_count:     200
    .vgpr_spill_count: 0
    .wavefront_size: 64
